# instruction warm-up: while waiting in each grid barrier waves 1..7 touch one dword per 128-B line of the next phase's code so its first-execution instruction fetches hit L2
# baseline (speedup 1.0000x reference)
.LBB0_391:
	s_waitcnt vmcnt(0)
	v_cmp_eq_u32_e32 vcc, 0, v0
	s_barrier
	s_cmp_eq_u32 s80, 0
	s_cbranch_scc1 .Lct_0
	s_cmp_gt_u32 s80, 3
	s_cbranch_scc1 .Lct_0
	s_getpc_b64 s[2:3]
	s_add_u32 s2, s2, 0xffffe31c
	s_addc_u32 s3, s3, -1
	s_lshl_b32 s32, s80, 13
	v_lshl_add_u32 v2, v170, 7, s32
	global_load_dword v3, v2, s[2:3]
.Lct_0:
	s_and_saveexec_b64 s[2:3], vcc
	s_cbranch_execz .LBB0_424
	s_lshl_b32 s4, s97, 8
	s_add_u32 s4, s70, s4
	s_addc_u32 s5, s71, 0
	v_mov_b32_e32 v1, 0x1000
	v_mov_b32_e32 v2, 1
	s_waitcnt vmcnt(0) expcnt(0) lgkmcnt(0)
	global_atomic_add v2, v1, v2, s[4:5] offset:1024 sc0
	v_cvt_f32_u32_e32 v1, s82
	s_sub_i32 s6, 0, s82
	v_rcp_iflag_f32_e32 v1, v1
	s_nop 0
	v_mul_f32_e32 v1, 0x4f7ffffe, v1
	v_cvt_u32_f32_e32 v1, v1
	v_mul_lo_u32 v3, s6, v1
	v_mul_hi_u32 v3, v1, v3
	v_add_u32_e32 v1, v1, v3
	s_waitcnt vmcnt(0)
	v_mul_hi_u32 v1, v2, v1
	v_mul_lo_u32 v3, v1, s82
	v_sub_u32_e32 v3, v2, v3
	v_add_u32_e32 v4, 1, v1
	v_cmp_le_u32_e32 vcc, s82, v3
	v_add_u32_e32 v2, 1, v2
	s_nop 0
	v_cndmask_b32_e32 v1, v1, v4, vcc
	v_subrev_u32_e32 v4, s82, v3
	v_cndmask_b32_e32 v3, v3, v4, vcc
	v_add_u32_e32 v4, 1, v1
	v_cmp_le_u32_e32 vcc, s82, v3
	s_nop 1
	v_cndmask_b32_e32 v1, v1, v4, vcc
	v_mul_lo_u32 v3, s82, v1
	v_add_u32_e32 v3, s82, v3
	v_cmp_ne_u32_e32 vcc, v2, v3
	s_and_saveexec_b64 s[6:7], vcc
	s_xor_b64 s[6:7], exec, s[6:7]
	s_cbranch_execz .LBB0_406
	v_mov_b32_e32 v2, 0x2000
	global_load_dword v2, v2, s[4:5] offset:1024 sc1
	s_add_u32 s10, s4, 0x2400
	s_addc_u32 s11, s5, 0
	s_waitcnt vmcnt(0)
	v_cmp_eq_u32_e32 vcc, v2, v1
	s_and_saveexec_b64 s[8:9], vcc
	s_cbranch_execz .LBB0_405
	s_mov_b32 s24, 1
	s_mov_b64 s[14:15], 0
	v_mov_b32_e32 v2, 0
	s_branch .LBB0_396

.LBB0_425:
	s_waitcnt vmcnt(0)
	s_cmp_lt_i32 s92, 3
	s_cselect_b64 s[10:11], -1, 0
	s_and_b64 s[0:1], s[10:11], s[0:1]
	s_andn2_b64 vcc, exec, s[0:1]
	s_cbranch_vccnz .LBB0_820
	s_and_b32 s1, s96, 7
	s_ashr_i32 s2, s72, 3
	s_mul_i32 s1, s1, s2
	s_ashr_i32 s2, s96, 3
	s_and_b32 s0, s72, 7
	s_add_i32 s2, s2, s1
	s_cmp_eq_u32 s0, 0
	s_cselect_b32 s27, s2, s96
	s_cmpk_gt_i32 s27, 0x1ff
	s_mov_b32 s15, 0
	s_cbranch_scc1 .LBB0_819
	s_add_u32 s16, s70, 0x38000
	s_addc_u32 s17, s71, 0
	s_add_u32 s18, s70, 0x2038000
	s_addc_u32 s19, s71, 0
	s_add_u32 s20, s70, 0x4038000
	v_lshrrev_b32_e32 v155, 4, v170
	v_lshrrev_b32_e32 v2, 1, v0
	s_addc_u32 s21, s71, 0
	v_bfe_u32 v3, v0, 1, 3
	v_bitop3_b32 v2, v155, v2, 7 bitop3:0x78
	s_add_u32 s22, s70, 0x5038000
	v_lshlrev_b32_e32 v159, 4, v2
	v_bitop3_b32 v2, v155, v3, 4 bitop3:0x36
	s_addc_u32 s23, s71, 0
	v_lshlrev_b32_e32 v160, 4, v2
	v_bfe_u32 v2, v0, 2, 2
	v_lshrrev_b32_e32 v3, 2, v170
	s_add_u32 s24, s70, 0x6038000
	s_movk_i32 s0, 0x70
	v_and_or_b32 v3, v3, 4, v2
	v_lshlrev_b32_e32 v5, 9, v2
	v_lshlrev_b32_e32 v2, 3, v0
	s_waitcnt vmcnt(7)
	v_and_b32_e32 v6, 31, v0
	s_addc_u32 s25, s71, 0
	v_bitop3_b32 v154, v158, s0, v0 bitop3:0x48
	v_lshrrev_b32_e32 v156, 5, v170
	v_and_b32_e32 v157, 0x1f0, v158
	v_lshlrev_b32_e32 v4, 12, v155
	v_lshlrev_b32_e32 v161, 5, v3
	v_and_b32_e32 v3, 24, v2
	v_lshlrev_b32_e32 v2, 3, v6
	s_add_u32 s36, s70, 0x1f168000
	v_and_b32_e32 v1, 15, v0
	v_lshrrev_b32_e32 v149, 3, v0
	v_lshl_or_b32 v162, v156, 13, v157
	v_mov_b32_e32 v147, 0
	v_or_b32_e32 v163, 0x40000, v154
	v_or_b32_e32 v164, 0xc0000, v154
	s_addc_u32 s37, s71, 0
	v_lshl_add_u32 v148, v6, 4, 0
	v_or3_b32 v165, v4, v5, v3
	v_or_b32_e32 v166, 0xc0100, v154
	s_add_i32 s38, 0, 0x20000
	s_movk_i32 s39, 0x3ff
	s_movk_i32 s40, 0xff80
	s_movk_i32 s41, 0x7ff
	s_movk_i32 s42, 0xbff
	s_mov_b32 s26, 0x3e38aa3b
	s_movk_i32 s43, 0x210
	s_movk_i32 s44, 0x800
	s_movk_i32 s45, 0xe800
	v_lshlrev_b32_e32 v150, 1, v2
	v_mov_b32_e32 v167, 0x3e38aa3b
	s_mov_b32 s0, s27
	s_mov_b32 s46, 0
	s_waitcnt vmcnt(0)
	s_branch .LBB0_429

.LBB0_837:
	s_waitcnt vmcnt(0)
	v_cmp_eq_u32_e32 vcc, 0, v0
	s_barrier
	s_cmp_eq_u32 s80, 0
	s_cbranch_scc1 .Lct_1
	s_cmp_gt_u32 s80, 7
	s_cbranch_scc1 .Lct_1
	s_getpc_b64 s[2:3]
	s_add_u32 s2, s2, 0xffffe31c
	s_addc_u32 s3, s3, -1
	s_lshl_b32 s32, s80, 13
	v_lshl_add_u32 v2, v170, 7, s32
	global_load_dword v3, v2, s[2:3]

.LBB0_871:
	s_waitcnt vmcnt(0)
	s_cmp_lt_i32 s92, 4
	s_cselect_b64 s[14:15], -1, 0
	s_and_b64 s[0:1], s[14:15], s[0:1]
	s_andn2_b64 vcc, exec, s[0:1]
	s_cbranch_vccnz .LBB0_983
	v_lshrrev_b32_e32 v155, 4, v170
	v_lshrrev_b32_e32 v152, 1, v0
	v_bfe_u32 v2, v0, 1, 3
	v_bitop3_b32 v3, v155, v152, 7 bitop3:0x78
	v_bitop3_b32 v2, v155, v2, 4 bitop3:0x36
	v_bfe_u32 v163, v0, 2, 2
	v_lshlrev_b32_e32 v146, 2, v155
	s_cmpk_gt_i32 s96, 0x7f
	v_lshlrev_b32_e32 v159, 4, v3
	v_lshlrev_b32_e32 v156, 4, v2
	v_and_or_b32 v2, v146, 4, v163
	v_lshlrev_b32_e32 v3, 9, v163
	v_lshlrev_b32_e32 v153, 3, v0
	s_cselect_b64 s[16:17], -1, 0
	v_lshrrev_b32_e32 v147, 3, v0
	v_and_b32_e32 v154, 15, v0
	v_lshrrev_b32_e32 v1, 5, v170
	v_and_b32_e32 v157, 0x1f0, v158
	v_lshl_or_b32 v160, v155, 12, v3
	v_lshlrev_b32_e32 v161, 5, v2
	v_and_b32_e32 v162, 24, v153
	s_and_b64 vcc, exec, s[16:17]
	s_cbranch_vccnz .LBB0_880
	s_add_u32 s19, s70, 0x9038000
	s_addc_u32 s21, s71, 0
	s_add_u32 s28, s70, 0x2038000
	s_addc_u32 s29, s71, 0
	s_add_u32 s30, s70, 0x1d958000
	s_addc_u32 s31, s71, 0
	s_movk_i32 s0, 0x70
	s_cmpk_lt_u32 s78, 0x100
	v_bitop3_b32 v150, v158, s0, v0 bitop3:0x48
	s_cselect_b64 s[0:1], -1, 0
	s_add_u32 s4, s70, 0x1f158000
	s_addc_u32 s5, s71, 0
	s_bfe_u32 s2, s78, 0x10006
	s_lshl_b32 s34, s2, 12
	s_cmp_eq_u32 s2, 0
	s_cselect_b64 s[8:9], -1, 0
	s_lshl_b32 s2, s2, 7
	v_or_b32_e32 v2, s2, v170
	s_and_b32 s35, s78, 0x80
	v_lshl_add_u32 v166, v2, 1, 0
	v_lshlrev_b32_e32 v2, 10, v147
	s_mov_b32 s3, 0x30100
	s_add_u32 s36, s70, 0x1e158000
	v_or3_b32 v168, v2, v150, s3
	v_cndmask_b32_e64 v2, 0, 1, s[0:1]
	v_lshl_or_b32 v151, v1, 9, v157
	v_or_b32_e32 v164, 0x10000, v150
	v_or_b32_e32 v165, 0x30000, v150
	s_mov_b32 s7, 0
	v_mov_b32_e32 v149, 0
	s_addc_u32 s37, s71, 0
	v_or_b32_e32 v167, v160, v162
	s_lshl_b32 s38, s96, 8
	s_lshl_b32 s39, s72, 8
	s_add_i32 s40, 0, 0x18000
	s_movk_i32 s41, 0x210
	s_lshl_b32 s42, s2, 1
	v_lshlrev_b32_e32 v148, 1, v170
	s_mov_b64 s[10:11], 0x2038200
	s_mov_b32 s43, 0x2038000
	s_movk_i32 s44, 0x7f0
	s_mov_b32 s18, 0x3d372713
	s_mov_b32 s20, 0xc0135761
	s_add_i32 s45, 0, 0x10000
	s_add_i32 s46, 0, 0x20000
	v_cmp_ne_u32_e64 s[0:1], 1, v2
	s_mov_b32 s47, s96

.LBB0_1000:
	s_waitcnt vmcnt(0)
	v_cmp_eq_u32_e32 vcc, 0, v0
	s_barrier
	s_cmp_eq_u32 s80, 0
	s_cbranch_scc1 .Lct_2
	s_cmp_gt_u32 s80, 6
	s_cbranch_scc1 .Lct_2
	s_getpc_b64 s[0:1]
	s_add_u32 s0, s0, 0x24f4
	s_addc_u32 s1, s1, 0
	s_lshl_b32 s32, s80, 13
	v_lshl_add_u32 v2, v170, 7, s32
	global_load_dword v3, v2, s[0:1]
.Lct_2:
	s_and_saveexec_b64 s[0:1], vcc
	s_cbranch_execz .LBB0_1033
	s_lshl_b32 s2, s97, 8
	s_add_u32 s2, s70, s2
	s_addc_u32 s3, s71, 0
	v_mov_b32_e32 v1, 0x1000
	s_waitcnt vmcnt(23)
	v_mov_b32_e32 v2, 1
	s_waitcnt vmcnt(0) expcnt(0) lgkmcnt(0)
	global_atomic_add v2, v1, v2, s[2:3] offset:1024 sc0
	v_cvt_f32_u32_e32 v1, s82
	s_sub_i32 s6, 0, s82
	v_rcp_iflag_f32_e32 v1, v1
	s_nop 0
	v_mul_f32_e32 v1, 0x4f7ffffe, v1
	v_cvt_u32_f32_e32 v1, v1
	v_mul_lo_u32 v3, s6, v1
	v_mul_hi_u32 v3, v1, v3
	v_add_u32_e32 v1, v1, v3
	s_waitcnt vmcnt(0)
	v_mul_hi_u32 v1, v2, v1
	v_mul_lo_u32 v3, v1, s82
	v_sub_u32_e32 v3, v2, v3
	v_add_u32_e32 v4, 1, v1
	v_cmp_le_u32_e32 vcc, s82, v3
	v_add_u32_e32 v2, 1, v2
	s_nop 0
	v_cndmask_b32_e32 v1, v1, v4, vcc
	v_subrev_u32_e32 v4, s82, v3
	v_cndmask_b32_e32 v3, v3, v4, vcc
	v_add_u32_e32 v4, 1, v1
	v_cmp_le_u32_e32 vcc, s82, v3
	s_nop 1
	v_cndmask_b32_e32 v1, v1, v4, vcc
	v_mul_lo_u32 v3, s82, v1
	v_add_u32_e32 v3, s82, v3
	v_cmp_ne_u32_e32 vcc, v2, v3
	s_and_saveexec_b64 s[6:7], vcc
	s_xor_b64 s[6:7], exec, s[6:7]
	s_cbranch_execz .LBB0_1015
	v_mov_b32_e32 v2, 0x2000
	global_load_dword v2, v2, s[2:3] offset:1024 sc1
	s_add_u32 s10, s2, 0x2400
	s_addc_u32 s11, s3, 0
	s_waitcnt vmcnt(0)
	v_cmp_eq_u32_e32 vcc, v2, v1
	s_and_saveexec_b64 s[8:9], vcc
	s_cbranch_execz .LBB0_1014
	s_mov_b32 s24, 1
	s_mov_b64 s[14:15], 0
	v_mov_b32_e32 v2, 0
	s_branch .LBB0_1005

.LBB0_1034:
	s_waitcnt vmcnt(0)
	s_cmp_gt_i32 s92, 6
	s_cselect_b64 s[0:1], -1, 0
	s_cmp_lt_i32 s93, 7
	s_cselect_b64 s[2:3], -1, 0
	s_or_b64 s[0:1], s[0:1], s[2:3]
	s_cmpk_eq_i32 s72, 0x100
	s_cselect_b64 s[76:77], -1, 0
	s_or_b64 s[0:1], s[0:1], s[76:77]
	s_and_b64 vcc, exec, s[0:1]
	s_cbranch_vccnz .LBB0_1123
	s_and_b32 s1, s96, 7
	s_ashr_i32 s2, s72, 3
	s_mul_i32 s1, s1, s2
	s_ashr_i32 s2, s96, 3
	s_and_b32 s0, s72, 7
	s_add_i32 s2, s2, s1
	s_cmp_eq_u32 s0, 0
	s_cselect_b32 s15, s2, s96
	s_cmpk_gt_i32 s15, 0x7f
	s_mov_b32 s3, 0
	s_cbranch_scc1 .LBB0_1072
	v_lshrrev_b32_e32 v252, 4, v170
	s_waitcnt vmcnt(23)
	v_lshrrev_b32_e32 v2, 1, v0
	s_add_u32 s6, s70, 0x9038000
	v_bfe_u32 v3, v0, 1, 3
	v_bitop3_b32 v2, v252, v2, 7 bitop3:0x78
	s_addc_u32 s7, s71, 0
	v_lshlrev_b32_e32 v209, 4, v2
	v_bitop3_b32 v2, v252, v3, 4 bitop3:0x36
	s_add_u32 s8, s70, 0xc038000
	v_lshlrev_b32_e32 v206, 4, v2
	v_bfe_u32 v2, v0, 2, 2
	v_lshrrev_b32_e32 v3, 2, v170
	s_addc_u32 s9, s71, 0
	v_and_or_b32 v3, v3, 4, v2
	v_lshlrev_b32_e32 v5, 9, v2
	v_lshlrev_b32_e32 v2, 3, v0
	s_waitcnt vmcnt(7)
	v_and_b32_e32 v6, 31, v0
	s_add_u32 s10, s70, 0xa038000
	s_movk_i32 s0, 0x70
	v_lshlrev_b32_e32 v207, 5, v3
	v_and_b32_e32 v3, 24, v2
	v_lshlrev_b32_e32 v2, 3, v6
	s_addc_u32 s11, s71, 0
	v_bitop3_b32 v171, v158, s0, v0 bitop3:0x48
	v_lshrrev_b32_e32 v253, 5, v170
	v_and_b32_e32 v254, 0x1f0, v158
	v_lshlrev_b32_e32 v4, 12, v252
	s_add_u32 s16, s70, 0x20168000
	v_lshlrev_b32_e32 v146, 1, v2
	v_mbcnt_lo_u32_b32 v2, -1, 0
	v_and_b32_e32 v1, 15, v0
	v_lshrrev_b32_e32 v159, 3, v0
	v_lshl_or_b32 v208, v253, 11, v254
	v_mov_b32_e32 v147, 0
	v_cmp_eq_u32_e32 vcc, 0, v6
	v_or_b32_e32 v210, 0x60000, v171
	s_addc_u32 s17, s71, 0
	v_lshl_add_u32 v211, v6, 4, 0
	v_or3_b32 v212, v4, v5, v3
	v_or_b32_e32 v213, 0x60100, v171
	s_movk_i32 s18, 0x210
	s_mov_b32 s14, 0xbfb8aa3b
	v_mbcnt_hi_u32_b32 v214, -1, v2
	s_mov_b32 s0, s15
	s_mov_b32 s19, 0
	s_branch .LBB0_1038

.LBB0_1255:
	s_waitcnt vmcnt(0)
	v_cmp_eq_u32_e32 vcc, 0, v0
	s_barrier
	s_cmp_eq_u32 s80, 0
	s_cbranch_scc1 .Lct_3
	s_cmp_gt_u32 s80, 2
	s_cbranch_scc1 .Lct_3
	s_getpc_b64 s[2:3]
	s_add_u32 s2, s2, 0xffffe320
	s_addc_u32 s3, s3, -1
	s_lshl_b32 s32, s80, 13
	v_lshl_add_u32 v2, v170, 7, s32
	global_load_dword v3, v2, s[2:3]
.Lct_3:
	s_and_saveexec_b64 s[2:3], vcc
	s_cbranch_execz .LBB0_1288
	s_lshl_b32 s4, s97, 8
	s_add_u32 s4, s70, s4
	s_addc_u32 s5, s71, 0
	v_mov_b32_e32 v1, 0x1000
	s_waitcnt vmcnt(23)
	v_mov_b32_e32 v2, 1
	s_waitcnt vmcnt(0) expcnt(0) lgkmcnt(0)
	global_atomic_add v2, v1, v2, s[4:5] offset:1024 sc0
	v_cvt_f32_u32_e32 v1, s82
	s_sub_i32 s6, 0, s82
	v_rcp_iflag_f32_e32 v1, v1
	s_nop 0
	v_mul_f32_e32 v1, 0x4f7ffffe, v1
	v_cvt_u32_f32_e32 v1, v1
	v_mul_lo_u32 v3, s6, v1
	v_mul_hi_u32 v3, v1, v3
	v_add_u32_e32 v1, v1, v3
	s_waitcnt vmcnt(0)
	v_mul_hi_u32 v1, v2, v1
	v_mul_lo_u32 v3, v1, s82
	v_sub_u32_e32 v3, v2, v3
	v_add_u32_e32 v4, 1, v1
	v_cmp_le_u32_e32 vcc, s82, v3
	v_add_u32_e32 v2, 1, v2
	s_nop 0
	v_cndmask_b32_e32 v1, v1, v4, vcc
	v_subrev_u32_e32 v4, s82, v3
	v_cndmask_b32_e32 v3, v3, v4, vcc
	v_add_u32_e32 v4, 1, v1
	v_cmp_le_u32_e32 vcc, s82, v3
	s_nop 1
	v_cndmask_b32_e32 v1, v1, v4, vcc
	v_mul_lo_u32 v3, s82, v1
	v_add_u32_e32 v3, s82, v3
	v_cmp_ne_u32_e32 vcc, v2, v3
	s_and_saveexec_b64 s[6:7], vcc
	s_xor_b64 s[6:7], exec, s[6:7]
	s_cbranch_execz .LBB0_1270
	v_mov_b32_e32 v2, 0x2000
	global_load_dword v2, v2, s[4:5] offset:1024 sc1
	s_add_u32 s10, s4, 0x2400
	s_addc_u32 s11, s5, 0
	s_waitcnt vmcnt(0)
	v_cmp_eq_u32_e32 vcc, v2, v1
	s_and_saveexec_b64 s[8:9], vcc
	s_cbranch_execz .LBB0_1269
	s_mov_b32 s22, 1
	s_mov_b64 s[12:13], 0
	v_mov_b32_e32 v2, 0
	s_branch .LBB0_1260

.LBB0_1289:
	s_waitcnt vmcnt(0)
	s_cmp_lt_i32 s92, 11
	s_cselect_b64 s[2:3], -1, 0
	s_and_b64 s[0:1], s[2:3], s[0:1]
	s_andn2_b64 vcc, exec, s[0:1]
	s_cbranch_vccnz .LBB0_1362
	s_cmp_gt_i32 s96, 63
	s_cbranch_scc1 .LBB0_1361
	s_waitcnt vmcnt(23)
	v_mbcnt_lo_u32_b32 v2, -1, 0
	v_mbcnt_hi_u32_b32 v2, -1, v2
	v_and_b32_e32 v3, 64, v2
	v_add_u32_e32 v4, -1, v2
	v_cmp_lt_i32_e32 vcc, v4, v3
	s_add_u32 s56, s70, 0x140b8000
	s_addc_u32 s57, s71, 0
	v_cndmask_b32_e32 v4, v4, v2, vcc
	s_waitcnt vmcnt(4)
	v_lshlrev_b32_e32 v19, 2, v4
	v_add_u32_e32 v4, -2, v2
	v_cmp_lt_i32_e32 vcc, v4, v3
	s_add_u32 s58, s70, 0x140c8000
	s_addc_u32 s59, s71, 0
	v_cndmask_b32_e32 v4, v4, v2, vcc
	v_lshlrev_b32_e32 v20, 2, v4
	v_add_u32_e32 v4, -4, v2
	v_cmp_lt_i32_e32 vcc, v4, v3
	s_cmp_lt_u32 s78, 64
	s_cselect_b64 s[74:75], -1, 0
	v_cndmask_b32_e32 v4, v4, v2, vcc
	v_lshlrev_b32_e32 v21, 2, v4
	v_add_u32_e32 v4, -8, v2
	v_cmp_lt_i32_e32 vcc, v4, v3
	s_lshl_b32 s18, s80, 2
	s_add_i32 s83, s18, 0
	v_cndmask_b32_e32 v4, v4, v2, vcc
	s_waitcnt vmcnt(3)
	v_lshlrev_b32_e32 v22, 2, v4
	v_add_u32_e32 v4, -16, v2
	v_cmp_lt_i32_e32 vcc, v4, v3
	s_cmpk_gt_u32 s78, 0x7f
	s_cselect_b64 s[18:19], -1, 0
	v_cndmask_b32_e32 v4, v4, v2, vcc
	v_lshlrev_b32_e32 v23, 2, v4
	v_subrev_u32_e32 v4, 32, v2
	v_cmp_lt_i32_e32 vcc, v4, v3
	s_cmpk_gt_u32 s78, 0xbf
	s_cselect_b64 s[20:21], -1, 0
	v_cndmask_b32_e32 v3, v4, v2, vcc
	v_lshlrev_b32_e32 v24, 2, v3
	s_cmpk_gt_u32 s78, 0xff
	v_and_b32_e32 v3, 63, v2
	s_cselect_b64 s[22:23], -1, 0
	s_cmpk_gt_u32 s78, 0x13f
	v_cmp_ne_u32_e32 vcc, 63, v3
	s_cselect_b64 s[24:25], -1, 0
	s_cmpk_gt_u32 s78, 0x17f
	v_addc_co_u32_e32 v4, vcc, 0, v2, vcc
	s_cselect_b64 s[26:27], -1, 0
	s_cmpk_gt_u32 s78, 0x1bf
	v_cmp_gt_u32_e32 vcc, 62, v3
	s_cselect_b64 s[28:29], -1, 0
	s_cmpk_gt_u32 s78, 0x1ff
	v_lshlrev_b32_e32 v25, 2, v4
	v_cndmask_b32_e64 v4, 0, 2, vcc
	v_cmp_gt_u32_e32 vcc, 60, v3
	s_cselect_b64 s[30:31], -1, 0
	s_waitcnt vmcnt(2)
	v_add_lshl_u32 v26, v4, v2, 2
	v_cndmask_b32_e64 v4, 0, 4, vcc
	v_cmp_gt_u32_e32 vcc, 56, v3
	s_mov_b32 s44, s97
	s_ashr_i32 s97, s96, 31
	v_add_lshl_u32 v27, v4, v2, 2
	v_cndmask_b32_e64 v4, 0, 8, vcc
	v_cmp_gt_u32_e32 vcc, 48, v3
	s_lshl_b32 s85, s96, 8
	s_lshl_b32 s86, s72, 8
	s_lshl_b64 s[42:43], s[96:97], 13
	v_cndmask_b32_e64 v3, 0, 16, vcc
	s_add_u32 s42, s70, s42
	v_add_lshl_u32 v29, v3, v2, 2
	v_mov_b32_e32 v3, 0x80
	v_mov_b32_e32 v159, 0
	s_addc_u32 s43, s71, s43
	v_add_lshl_u32 v28, v4, v2, 2
	v_lshl_or_b32 v30, v2, 2, v3
	v_lshl_add_u64 v[2:3], s[42:43], 0, v[158:159]
	s_mov_b64 s[42:43], 0x140d800c
	v_lshlrev_b32_e32 v1, 2, v0
	s_movk_i32 s33, 0x100
	v_lshl_add_u64 v[10:11], v[2:3], 0, s[42:43]
	s_ashr_i32 s73, s72, 31
	v_cndmask_b32_e64 v2, 0, 1, s[74:75]
	v_cmp_gt_u32_e64 s[0:1], s33, v0
	v_add_u32_e32 v16, 0, v1
	v_lshlrev_b32_e32 v17, 2, v170
	v_lshl_add_u32 v18, v170, 4, 0
	v_cmp_eq_u32_e64 s[4:5], 0, v170
	v_cmp_gt_u32_e64 s[6:7], 2, v170
	v_cmp_gt_u32_e64 s[8:9], 4, v170
	v_cmp_gt_u32_e64 s[10:11], 8, v170
	v_cmp_gt_u32_e64 s[12:13], 16, v170
	v_cmp_gt_u32_e64 s[14:15], 32, v170
	v_cmp_eq_u32_e64 s[16:17], 63, v170
	s_movk_i32 s84, 0xff
	v_cmp_gt_u32_e64 s[34:35], 62, v170
	v_cmp_gt_u32_e64 s[36:37], 60, v170
	v_cmp_gt_u32_e64 s[38:39], 56, v170
	v_cmp_gt_u32_e64 s[40:41], 48, v170
	v_or_b32_e32 v31, 1, v1
	v_or_b32_e32 v32, 2, v1
	v_or_b32_e32 v33, 3, v1
	s_mov_b32 s97, s44
	s_lshl_b64 s[78:79], s[72:73], 13
	v_mov_b32_e32 v34, 1
	v_cmp_ne_u32_e64 s[42:43], 1, v2
	s_mov_b32 s73, s96
	s_branch .LBB0_1293

.LBB0_1383:
	s_waitcnt vmcnt(0)
	v_cmp_eq_u32_e32 vcc, 0, v0
	s_barrier
	s_cmp_eq_u32 s80, 0
	s_cbranch_scc1 .Lct_4
	s_cmp_gt_u32 s80, 4
	s_cbranch_scc1 .Lct_4
	s_getpc_b64 s[2:3]
	s_add_u32 s2, s2, 0xffffe320
	s_addc_u32 s3, s3, -1
	s_lshl_b32 s32, s80, 13
	v_lshl_add_u32 v2, v170, 7, s32
	global_load_dword v3, v2, s[2:3]

.LBB0_1417:
	s_waitcnt vmcnt(0)
	s_cmp_lt_i32 s92, 12
	s_cselect_b64 s[8:9], -1, 0
	s_and_b64 s[0:1], s[8:9], s[0:1]
	s_andn2_b64 vcc, exec, s[0:1]
	s_cbranch_vccnz .LBB0_1482
	s_and_b32 s2, s96, 7
	s_ashr_i32 s3, s72, 3
	s_mul_i32 s2, s2, s3
	s_ashr_i32 s5, s96, 3
	s_and_b32 s4, s72, 7
	s_add_i32 s6, s5, s2
	s_and_b32 s2, s96, 4
	s_bfe_i32 s3, s96, 0x10002
	s_bitcmp1_b32 s96, 2
	s_cselect_b64 s[12:13], -1, 0
	s_lshl_b32 s7, s96, 5
	s_and_b32 s7, s7, 0xe0
	s_add_i32 s7, s5, s7
	s_cmp_eq_u32 s2, 0
	s_cselect_b64 s[14:15], -1, 0
	s_and_b32 s42, s3, 0x480
	s_add_u32 s16, s70, 0x140b8000
	s_addc_u32 s17, s71, 0
	s_add_u32 s18, s70, 0x12038000
	v_lshrrev_b32_e32 v192, 4, v170
	v_lshrrev_b32_e32 v195, 1, v0
	s_waitcnt vmcnt(23)
	v_bfe_u32 v3, v0, 1, 3
	s_addc_u32 s19, s71, 0
	v_bitop3_b32 v4, v192, v195, 7 bitop3:0x78
	v_bitop3_b32 v3, v192, v3, 4 bitop3:0x36
	s_add_u32 s43, s70, 0x14158000
	v_lshlrev_b32_e32 v196, 4, v4
	v_lshlrev_b32_e32 v197, 4, v3
	v_bfe_u32 v3, v0, 2, 2
	v_lshrrev_b32_e32 v4, 2, v170
	s_addc_u32 s44, s71, 0
	s_waitcnt vmcnt(7)
	v_lshrrev_b32_e32 v6, 4, v0
	v_and_or_b32 v4, v4, 4, v3
	s_add_u32 s45, s70, 0x7038000
	v_xor_b32_e32 v6, v6, v0
	v_lshrrev_b32_e32 v193, 5, v170
	v_lshlrev_b32_e32 v198, 5, v4
	v_lshlrev_b32_e32 v4, 3, v0
	s_addc_u32 s46, s71, 0
	v_lshlrev_b32_e32 v6, 3, v6
	v_and_b32_e32 v2, 31, v0
	v_and_b32_e32 v8, 24, v4
	v_mul_u32_u24_e32 v4, 0x2c00, v193
	s_add_u32 s47, s70, 0x4000
	v_and_b32_e32 v201, 56, v6
	v_and_b32_e32 v6, 2, v0
	v_lshl_or_b32 v199, v2, 4, v4
	s_addc_u32 s48, s71, 0
	s_ashr_i32 s2, s7, 5
	v_lshlrev_b32_e32 v4, 6, v0
	v_mov_b32_e32 v7, s63
	v_mov_b32_e32 v9, s61
	v_cmp_eq_u32_e32 vcc, 0, v6
	s_mul_hi_i32 s3, s2, 0x1600000
	s_mul_i32 s2, s2, 0x1600000
	v_and_b32_e32 v4, 64, v4
	v_cndmask_b32_e32 v177, v7, v9, vcc
	v_mov_b32_e32 v6, s62
	v_mov_b32_e32 v7, s60
	v_mov_b32_e32 v173, 0
	s_add_u32 s2, s64, s2
	v_lshlrev_b32_e32 v172, 1, v4
	v_cndmask_b32_e32 v176, v6, v7, vcc
	v_lshlrev_b32_e32 v6, 12, v0
	s_addc_u32 s3, s65, s3
	s_lshl_b32 s5, s5, 8
	v_lshl_add_u64 v[174:175], s[18:19], 0, v[172:173]
	v_and_b32_e32 v172, 0x1fe000, v6
	v_and_b32_e32 v1, 15, v0
	s_mov_b32 s11, 0
	s_and_b32 s10, s5, 0x1c00
	v_lshl_add_u64 v[6:7], s[2:3], 0, v[172:173]
	v_lshlrev_b32_e32 v9, 9, v0
	v_lshrrev_b32_e32 v171, 3, v0
	s_movk_i32 s0, 0x70
	v_lshlrev_b32_e32 v194, 3, v2
	v_lshlrev_b32_e32 v5, 12, v192
	v_lshlrev_b32_e32 v3, 9, v3
	v_lshlrev_b32_e32 v2, 3, v1
	s_cmp_eq_u32 s4, 0
	v_lshl_add_u64 v[6:7], v[6:7], 0, s[10:11]
	v_and_b32_e32 v172, 0x200, v9
	v_bitop3_b32 v190, v158, s0, v0 bitop3:0x48
	v_or_b32_e32 v191, 0x80, v171
	v_cmp_eq_u32_e64 s[0:1], 0, v0
	v_or_b32_e32 v202, 0xc0, v171
	v_lshl_add_u64 v[178:179], v[6:7], 0, v[172:173]
	s_cselect_b32 s49, s6, s96
	s_cselect_b32 s50, s7, s96
	v_or3_b32 v203, v5, v3, v8
	s_mov_b64 s[2:3], 0
	v_lshlrev_b32_e32 v180, 2, v4
	s_mov_b64 s[20:21], 0x80
	s_movk_i32 s51, 0xff
	s_add_i32 s52, 0, 0x18000
	s_mov_b32 s53, 0x10000
	s_add_i32 s56, 0, 0x20000
	s_movk_i32 s57, 0x110
	s_mov_b32 s10, 0xbfb8aa3b
	v_lshlrev_b32_e32 v182, 1, v2
	s_movk_i32 s58, 0x1600
	s_mov_b64 s[22:23], 0x10000
	v_mov_b32_e32 v208, 0
	v_mov_b32_e32 v209, 0
	v_mov_b32_e32 v210, 0
	v_mov_b32_e32 v211, 0
	s_branch .LBB0_1422

.LBB0_1499:
	s_waitcnt vmcnt(0)
	v_cmp_eq_u32_e32 vcc, 0, v0
	s_barrier
	s_cmp_eq_u32 s80, 0
	s_cbranch_scc1 .Lct_5
	s_cmp_gt_u32 s80, 2
	s_cbranch_scc1 .Lct_5
	s_getpc_b64 s[0:1]
	s_add_u32 s0, s0, 0xffffe320
	s_addc_u32 s1, s1, -1
	s_lshl_b32 s32, s80, 13
	v_lshl_add_u32 v2, v170, 7, s32
	global_load_dword v3, v2, s[0:1]
.Lct_5:
	s_and_saveexec_b64 s[0:1], vcc
	s_cbranch_execz .LBB0_1532
	s_lshl_b32 s4, s97, 8
	s_add_u32 s4, s70, s4
	s_addc_u32 s5, s71, 0
	v_mov_b32_e32 v1, 0x1000
	s_waitcnt vmcnt(23)
	v_mov_b32_e32 v2, 1
	s_waitcnt vmcnt(0) expcnt(0) lgkmcnt(0)
	global_atomic_add v2, v1, v2, s[4:5] offset:1024 sc0
	v_cvt_f32_u32_e32 v1, s82
	s_sub_i32 s6, 0, s82
	v_rcp_iflag_f32_e32 v1, v1
	s_nop 0
	v_mul_f32_e32 v1, 0x4f7ffffe, v1
	v_cvt_u32_f32_e32 v1, v1
	v_mul_lo_u32 v3, s6, v1
	v_mul_hi_u32 v3, v1, v3
	v_add_u32_e32 v1, v1, v3
	s_waitcnt vmcnt(0)
	v_mul_hi_u32 v1, v2, v1
	v_mul_lo_u32 v3, v1, s82
	v_sub_u32_e32 v3, v2, v3
	v_add_u32_e32 v4, 1, v1
	v_cmp_le_u32_e32 vcc, s82, v3
	v_add_u32_e32 v2, 1, v2
	s_nop 0
	v_cndmask_b32_e32 v1, v1, v4, vcc
	v_subrev_u32_e32 v4, s82, v3
	v_cndmask_b32_e32 v3, v3, v4, vcc
	v_add_u32_e32 v4, 1, v1
	v_cmp_le_u32_e32 vcc, s82, v3
	s_nop 1
	v_cndmask_b32_e32 v1, v1, v4, vcc
	v_mul_lo_u32 v3, s82, v1
	v_add_u32_e32 v3, s82, v3
	v_cmp_ne_u32_e32 vcc, v2, v3
	s_and_saveexec_b64 s[6:7], vcc
	s_xor_b64 s[6:7], exec, s[6:7]
	s_cbranch_execz .LBB0_1514
	v_mov_b32_e32 v2, 0x2000
	global_load_dword v2, v2, s[4:5] offset:1024 sc1
	s_add_u32 s10, s4, 0x2400
	s_addc_u32 s11, s5, 0
	s_waitcnt vmcnt(0)
	v_cmp_eq_u32_e32 vcc, v2, v1
	s_and_saveexec_b64 s[8:9], vcc
	s_cbranch_execz .LBB0_1513
	s_mov_b32 s22, 1
	s_mov_b64 s[12:13], 0
	v_mov_b32_e32 v2, 0
	s_branch .LBB0_1504

.LBB0_1533:
	s_waitcnt vmcnt(0)
	s_cmp_lt_i32 s92, 13
	s_cselect_b64 s[0:1], -1, 0
	s_and_b64 s[2:3], s[0:1], s[2:3]
	s_andn2_b64 vcc, exec, s[2:3]
	s_cbranch_vccnz .LBB0_1544
	s_and_b32 s3, s96, 7
	s_ashr_i32 s4, s72, 3
	s_mul_i32 s3, s3, s4
	s_ashr_i32 s4, s96, 3
	s_and_b32 s2, s72, 7
	s_add_i32 s4, s4, s3
	s_cmp_eq_u32 s2, 0
	s_cselect_b32 s18, s4, s96
	s_cmpk_gt_i32 s18, 0x1ff
	s_mov_b32 s3, 0
	s_cbranch_scc1 .LBB0_1543
	s_waitcnt vmcnt(23)
	v_lshrrev_b32_e32 v3, 4, v0
	v_xor_b32_e32 v2, v3, v0
	v_lshlrev_b32_e32 v2, 3, v2
	v_and_b32_e32 v177, 56, v2
	v_lshrrev_b32_e32 v193, 4, v170
	v_lshrrev_b32_e32 v195, 1, v0
	v_bfe_u32 v2, v0, 1, 3
	v_bitop3_b32 v4, v193, v195, 7 bitop3:0x78
	v_bitop3_b32 v2, v193, v2, 4 bitop3:0x36
	s_add_u32 s19, s70, 0x14158000
	v_lshlrev_b32_e32 v196, 4, v4
	v_lshlrev_b32_e32 v197, 4, v2
	v_bfe_u32 v2, v0, 2, 2
	v_lshrrev_b32_e32 v4, 2, v170
	s_addc_u32 s20, s71, 0
	v_and_or_b32 v4, v4, 4, v2
	s_waitcnt vmcnt(7)
	v_lshlrev_b32_e32 v7, 9, v2
	v_lshlrev_b32_e32 v2, 3, v0
	s_add_u32 s21, s70, 0x19958000
	v_lshlrev_b32_e32 v5, 12, v193
	v_and_b32_e32 v8, 24, v2
	v_and_b32_e32 v9, 31, v0
	s_addc_u32 s22, s71, 0
	v_lshlrev_b32_e32 v6, 6, v0
	s_waitcnt vmcnt(6)
	v_lshlrev_b32_e32 v10, 11, v0
	v_lshlrev_b32_e32 v198, 5, v4
	v_lshlrev_b32_e32 v2, 3, v9
	v_mov_b32_e32 v173, 0
	s_add_u32 s4, s70, 0x140c8000
	v_and_b32_e32 v4, 64, v6
	v_and_b32_e32 v172, 0xfe000, v10
	v_and_b32_e32 v6, 0xc0, v6
	v_or3_b32 v201, v5, v7, v8
	v_bitop3_b32 v3, v3, 7, v0 bitop3:0x48
	v_mov_b32_e32 v5, 0x108100
	v_and_b32_e32 v1, 15, v0
	v_lshrrev_b32_e32 v171, 3, v0
	v_or_b32_e32 v190, 0x2c000, v177
	v_or_b32_e32 v191, 0x58000, v177
	v_or_b32_e32 v192, 0x84000, v177
	v_lshlrev_b32_e32 v194, 3, v170
	v_lshlrev_b32_e32 v199, 4, v170
	v_lshrrev_b32_e32 v200, 5, v170
	s_addc_u32 s5, s71, 0
	v_lshl_add_u64 v[174:175], s[64:65], 0, v[172:173]
	v_lshl_add_u32 v176, v9, 4, 0
	v_lshl_or_b32 v202, v3, 4, v5
	v_lshlrev_b32_e32 v178, 1, v4
	v_lshlrev_b32_e32 v180, 2, v6
	s_mov_b64 s[6:7], 0x80
	v_mov_b32_e32 v203, 0x60
	s_movk_i32 s23, 0x80
	s_add_i32 s24, 0, 0x18000
	s_add_i32 s25, 0, 0x20000
	s_mov_b32 s26, 0x6050400
	s_movk_i32 s27, 0x210
	v_lshlrev_b32_e32 v182, 1, v2
	v_mov_b32_e32 v204, 0x1600000
	s_mov_b32 s16, s18
	s_mov_b32 s28, 0
	s_branch .LBB0_1537

.LBB0_1561:
	s_waitcnt vmcnt(0)
	v_cmp_eq_u32_e32 vcc, 0, v0
	s_barrier
	s_cmp_eq_u32 s80, 0
	s_cbranch_scc1 .Lct_6
	s_cmp_gt_u32 s80, 2
	s_cbranch_scc1 .Lct_6
	s_getpc_b64 s[0:1]
	s_add_u32 s0, s0, 0xffffe318
	s_addc_u32 s1, s1, -1
	s_lshl_b32 s32, s80, 13
	v_lshl_add_u32 v2, v170, 7, s32
	global_load_dword v3, v2, s[0:1]
.Lct_6:
	s_and_saveexec_b64 s[0:1], vcc
	s_cbranch_execz .LBB0_1594
	s_lshl_b32 s4, s97, 8
	s_add_u32 s4, s70, s4
	s_addc_u32 s5, s71, 0
	v_mov_b32_e32 v0, 0x1000
	v_mov_b32_e32 v1, 1
	s_waitcnt vmcnt(0) expcnt(0) lgkmcnt(0)
	global_atomic_add v1, v0, v1, s[4:5] offset:1024 sc0
	v_cvt_f32_u32_e32 v0, s82
	s_sub_i32 s6, 0, s82
	v_rcp_iflag_f32_e32 v0, v0
	s_nop 0
	v_mul_f32_e32 v0, 0x4f7ffffe, v0
	v_cvt_u32_f32_e32 v0, v0
	v_mul_lo_u32 v2, s6, v0
	v_mul_hi_u32 v2, v0, v2
	v_add_u32_e32 v0, v0, v2
	s_waitcnt vmcnt(0)
	v_mul_hi_u32 v0, v1, v0
	v_mul_lo_u32 v2, v0, s82
	v_sub_u32_e32 v2, v1, v2
	v_add_u32_e32 v3, 1, v0
	v_cmp_le_u32_e32 vcc, s82, v2
	v_add_u32_e32 v1, 1, v1
	s_nop 0
	v_cndmask_b32_e32 v0, v0, v3, vcc
	v_subrev_u32_e32 v3, s82, v2
	v_cndmask_b32_e32 v2, v2, v3, vcc
	v_add_u32_e32 v3, 1, v0
	v_cmp_le_u32_e32 vcc, s82, v2
	s_nop 1
	v_cndmask_b32_e32 v0, v0, v3, vcc
	v_mul_lo_u32 v2, s82, v0
	v_add_u32_e32 v2, s82, v2
	v_cmp_ne_u32_e32 vcc, v1, v2
	s_and_saveexec_b64 s[6:7], vcc
	s_xor_b64 s[6:7], exec, s[6:7]
	s_cbranch_execz .LBB0_1576
	v_mov_b32_e32 v1, 0x2000
	global_load_dword v1, v1, s[4:5] offset:1024 sc1
	s_add_u32 s10, s4, 0x2400
	s_addc_u32 s11, s5, 0
	s_waitcnt vmcnt(0)
	v_cmp_eq_u32_e32 vcc, v1, v0
	s_and_saveexec_b64 s[8:9], vcc
	s_cbranch_execz .LBB0_1575
	s_mov_b32 s22, 1
	s_mov_b64 s[12:13], 0
	v_mov_b32_e32 v1, 0
	s_branch .LBB0_1566

.LBB0_1595:
	s_waitcnt vmcnt(0)
	s_cmp_gt_i32 s92, 13
	s_cselect_b64 s[0:1], -1, 0
	s_xor_b64 s[2:3], s[2:3], -1
	s_or_b64 s[0:1], s[0:1], s[2:3]
	s_and_b64 vcc, exec, s[0:1]
	s_cbranch_vccnz .LBB0_1700
	s_lshl_b32 s0, s96, 3
	s_add_i32 s2, s0, s80
	s_cmpk_gt_i32 s2, 0x1fff
	s_cbranch_scc1 .LBB0_1699
	s_waitcnt vmcnt(1)
	v_mov_b32_e32 v65, 0
	v_lshlrev_b32_e32 v64, 4, v170
	v_lshl_add_u64 v[16:17], s[66:67], 0, v[64:65]
	v_add_co_u32_e32 v32, vcc, 0x1000, v16
	global_load_dwordx4 v[0:3], v64, s[66:67]
	global_load_dwordx4 v[4:7], v64, s[66:67] offset:1024
	global_load_dwordx4 v[8:11], v64, s[66:67] offset:2048
	global_load_dwordx4 v[12:15], v64, s[66:67] offset:3072
	v_addc_co_u32_e32 v33, vcc, 0, v17, vcc
	global_load_dwordx4 v[16:19], v[32:33], off
	global_load_dwordx4 v[20:23], v[32:33], off offset:1024
	global_load_dwordx4 v[24:27], v[32:33], off offset:2048
	global_load_dwordx4 v[28:31], v[32:33], off offset:3072
	v_mbcnt_lo_u32_b32 v32, -1, 0
	v_mbcnt_hi_u32_b32 v32, -1, v32
	v_and_b32_e32 v33, 64, v32
	v_add_u32_e32 v33, 64, v33
	v_xor_b32_e32 v34, 32, v32
	v_cmp_lt_i32_e32 vcc, v34, v33
	s_add_u32 s4, s70, 0x19958000
	s_addc_u32 s5, s71, 0
	v_cndmask_b32_e32 v34, v32, v34, vcc
	v_lshlrev_b32_e32 v67, 2, v34
	v_xor_b32_e32 v34, 16, v32
	v_cmp_lt_i32_e32 vcc, v34, v33
	v_lshlrev_b32_e32 v64, 3, v170
	v_lshlrev_b32_e32 v66, 2, v170
	v_cndmask_b32_e32 v34, v32, v34, vcc
	v_lshlrev_b32_e32 v171, 2, v34
	v_xor_b32_e32 v34, 8, v32
	v_cmp_lt_i32_e32 vcc, v34, v33
	s_add_u32 s8, s70, 0x140d8000
	s_mov_b64 s[10:11], 0xe038000
	v_cndmask_b32_e32 v34, v32, v34, vcc
	v_lshlrev_b32_e32 v186, 2, v34
	v_xor_b32_e32 v34, 4, v32
	v_cmp_lt_i32_e32 vcc, v34, v33
	s_movk_i32 s28, 0x1000
	s_mov_b32 s7, 0
	v_cndmask_b32_e32 v34, v32, v34, vcc
	v_lshlrev_b32_e32 v187, 2, v34
	v_xor_b32_e32 v34, 2, v32
	v_cmp_lt_i32_e32 vcc, v34, v33
	s_addc_u32 s9, s71, 0
	s_lshl_b32 s29, s72, 3
	v_cndmask_b32_e32 v34, v32, v34, vcc
	v_lshlrev_b32_e32 v188, 2, v34
	v_xor_b32_e32 v34, 1, v32
	v_cmp_lt_i32_e32 vcc, v34, v33
	s_lshl_b32 s30, s72, 5
	v_cmp_gt_u32_e64 s[0:1], 16, v170
	v_cndmask_b32_e32 v32, v32, v34, vcc
	v_lshlrev_b32_e32 v189, 2, v32
	v_cmp_lt_u32_e32 vcc, 15, v170
	v_lshl_add_u64 v[32:33], s[70:71], 0, v[64:65]
	v_lshl_add_u64 v[68:69], v[32:33], 0, s[10:11]
	v_lshl_add_u64 v[70:71], s[4:5], 0, v[64:65]
	s_xor_b64 s[10:11], vcc, -1
	v_lshlrev_b32_e32 v64, 2, v66
	s_mov_b64 s[12:13], 0x12000
	s_mov_b32 s31, 0x12000
	v_mov_b32_e32 v190, 0x358637bd
	s_mov_b32 s33, 0x800000
	s_branch .LBB0_1601
